# baseline (speedup 1.0000x reference)
.LBB0_34:
	s_or_b64 exec, exec, s[10:11]
	ds_read_b128 v[18:21], v72
	s_waitcnt vmcnt(3)
	v_cvt_pk_f16_f32 v14, v14, v15
	v_cvt_pk_f16_f32 v15, v16, v17
	v_cvt_pk_f16_f32 v16, v10, v11
	ds_read_b128 v[22:25], v71 offset:41984
	v_cvt_pk_f16_f32 v17, v12, v13
	ds_read_b128 v[10:13], v72 offset:1024
	ds_read_b128 v[26:29], v71 offset:42048
	s_waitcnt vmcnt(1)
	v_cvt_pk_f16_f32 v0, v6, v7
	v_cvt_pk_f16_f32 v1, v8, v9
	v_cvt_pk_f16_f32 v2, v2, v3
	s_waitcnt lgkmcnt(2)
	v_mfma_f32_16x16x32_f16 v[30:33], v[18:21], v[14:17], v[22:25]
	v_cvt_pk_f16_f32 v3, v4, v5
	s_add_i32 s10, s20, s12
	s_nop 0
	v_mfma_f32_16x16x32_f16 v[18:21], v[18:21], v[0:3], v[22:25]
	ds_read_b128 v[4:7], v72 offset:2048
	s_nop 1
	ds_read_b128 v[22:25], v71 offset:42112
	s_waitcnt lgkmcnt(2)
	v_exp_f32_e32 v78, v30
	v_mfma_f32_16x16x32_f16 v[34:37], v[10:13], v[14:17], v[26:29]
	v_exp_f32_e32 v79, v31
	v_exp_f32_e32 v20, v20
	v_mfma_f32_16x16x32_f16 v[8:11], v[10:13], v[0:3], v[26:29]
	ds_read_b128 v[44:47], v71 offset:42176
	s_nop 3
	v_exp_f32_e64 v80, v34 clamp
	v_exp_f32_e64 v81, v35 clamp
	s_waitcnt lgkmcnt(1)
	v_mfma_f32_16x16x32_f16 v[48:51], v[4:7], v[14:17], v[22:25]
	ds_read_b128 v[26:29], v72 offset:3072
	v_exp_f32_e64 v82, v36 clamp
	v_exp_f32_e64 v83, v37 clamp
	v_exp_f32_e32 v21, v21
	v_mfma_f32_16x16x32_f16 v[22:25], v[4:7], v[0:3], v[22:25]
	ds_read_b128 v[52:55], v72 offset:4096
	ds_read_b128 v[56:59], v71 offset:42240
	s_nop 1
	v_exp_f32_e32 v4, v48
	s_waitcnt lgkmcnt(2)
	v_mfma_f32_16x16x32_f16 v[60:63], v[26:29], v[14:17], v[44:47]
	v_exp_f32_e32 v5, v49
	v_exp_f32_e32 v48, v32
	v_exp_f32_e32 v49, v33
	v_mfma_f32_16x16x32_f16 v[26:29], v[26:29], v[0:3], v[44:47]
	ds_read_b128 v[64:67], v71 offset:42304
	v_exp_f32_e32 v6, v50
	v_exp_f32_e32 v7, v51
	s_waitcnt lgkmcnt(1)
	v_mfma_f32_16x16x32_f16 v[74:77], v[52:55], v[14:17], v[56:59]
	ds_read_b128 v[44:47], v72 offset:5120
	v_exp_f32_e32 v50, v18
	v_exp_f32_e32 v51, v19
	v_exp_f32_e32 v26, v26
	v_mfma_f32_16x16x32_f16 v[30:33], v[52:55], v[0:3], v[56:59]
	v_exp_f32_e64 v52, v8 clamp
	v_exp_f32_e64 v53, v9 clamp
	v_exp_f32_e32 v8, v22
	s_waitcnt lgkmcnt(0)
	v_mfma_f32_16x16x32_f16 v[34:37], v[44:47], v[14:17], v[64:67]
	v_exp_f32_e32 v9, v23
	v_exp_f32_e64 v22, v10 clamp
	v_exp_f32_e64 v23, v11 clamp
	v_mfma_f32_16x16x32_f16 v[44:47], v[44:47], v[0:3], v[64:67]
	v_exp_f32_e32 v10, v24
	v_exp_f32_e32 v11, v25
	s_nop 1
	v_exp_f32_e32 v12, v34
	v_exp_f32_e32 v13, v35
	v_exp_f32_e32 v18, v36
	v_exp_f32_e32 v24, v60
	v_exp_f32_e32 v25, v61
	v_exp_f32_e64 v54, v74 clamp
	v_exp_f32_e64 v55, v75 clamp
	v_exp_f32_e32 v34, v62
	v_exp_f32_e32 v35, v63
	v_exp_f32_e64 v56, v76 clamp
	v_exp_f32_e64 v57, v77 clamp
	v_exp_f32_e32 v19, v37
	v_exp_f32_e32 v27, v27
	v_exp_f32_e64 v30, v30 clamp
	v_exp_f32_e64 v31, v31 clamp
	v_exp_f32_e32 v36, v44
	v_exp_f32_e32 v37, v45
	v_exp_f32_e32 v28, v28
	v_exp_f32_e32 v29, v29
	v_exp_f32_e64 v32, v32 clamp
	v_exp_f32_e64 v33, v33 clamp
	v_exp_f32_e32 v44, v46
	v_exp_f32_e32 v45, v47
	v_pk_fma_f32 v[58:59], v[80:81], s[2:3], 1.0 op_sel_hi:[1,0,0]
	v_pk_fma_f32 v[60:61], v[82:83], s[2:3], 1.0 op_sel_hi:[1,0,0]
	v_pk_fma_f32 v[52:53], v[52:53], s[2:3], 1.0 op_sel_hi:[1,0,0]
	v_pk_fma_f32 v[22:23], v[22:23], s[2:3], 1.0 op_sel_hi:[1,0,0]
	v_pk_fma_f32 v[54:55], v[54:55], s[2:3], 1.0 op_sel_hi:[1,0,0]
	v_pk_fma_f32 v[56:57], v[56:57], s[2:3], 1.0 op_sel_hi:[1,0,0]
	v_pk_fma_f32 v[30:31], v[30:31], s[2:3], 1.0 op_sel_hi:[1,0,0]
	v_pk_fma_f32 v[32:33], v[32:33], s[2:3], 1.0 op_sel_hi:[1,0,0]
	v_pk_fma_f32 v[46:47], v[78:79], v[58:59], v[58:59]
	v_pk_fma_f32 v[48:49], v[48:49], v[60:61], v[60:61]
	v_pk_fma_f32 v[50:51], v[50:51], v[52:53], v[52:53]
	v_pk_fma_f32 v[20:21], v[20:21], v[22:23], v[22:23]
	v_pk_fma_f32 v[24:25], v[24:25], v[54:55], v[54:55]
	v_pk_fma_f32 v[34:35], v[34:35], v[56:57], v[56:57]
	v_pk_fma_f32 v[26:27], v[26:27], v[30:31], v[30:31]
	v_pk_fma_f32 v[28:29], v[28:29], v[32:33], v[32:33]
	v_pk_fma_f32 v[58:59], v[58:59], s[6:7], v[40:41] op_sel_hi:[1,0,0] neg_lo:[1,0,0] neg_hi:[1,0,0]
	v_pk_fma_f32 v[60:61], v[60:61], s[6:7], v[40:41] op_sel_hi:[1,0,0] neg_lo:[1,0,0] neg_hi:[1,0,0]
	v_pk_fma_f32 v[52:53], v[52:53], s[6:7], v[40:41] op_sel_hi:[1,0,0] neg_lo:[1,0,0] neg_hi:[1,0,0]
	v_pk_fma_f32 v[22:23], v[22:23], s[6:7], v[40:41] op_sel_hi:[1,0,0] neg_lo:[1,0,0] neg_hi:[1,0,0]
	v_pk_fma_f32 v[54:55], v[54:55], s[6:7], v[40:41] op_sel_hi:[1,0,0] neg_lo:[1,0,0] neg_hi:[1,0,0]
	v_pk_fma_f32 v[56:57], v[56:57], s[6:7], v[40:41] op_sel_hi:[1,0,0] neg_lo:[1,0,0] neg_hi:[1,0,0]
	v_pk_fma_f32 v[30:31], v[30:31], s[6:7], v[40:41] op_sel_hi:[1,0,0] neg_lo:[1,0,0] neg_hi:[1,0,0]
	v_pk_fma_f32 v[32:33], v[32:33], s[6:7], v[40:41] op_sel_hi:[1,0,0] neg_lo:[1,0,0] neg_hi:[1,0,0]
	v_pk_fma_f32 v[46:47], v[4:5], v[46:47], v[46:47]
	v_pk_fma_f32 v[48:49], v[6:7], v[48:49], v[48:49]
	v_pk_fma_f32 v[50:51], v[8:9], v[50:51], v[50:51]
	v_pk_fma_f32 v[20:21], v[10:11], v[20:21], v[20:21]
	v_pk_fma_f32 v[24:25], v[12:13], v[24:25], v[24:25]
	v_pk_fma_f32 v[34:35], v[18:19], v[34:35], v[34:35]
	v_pk_fma_f32 v[26:27], v[36:37], v[26:27], v[26:27]
	v_pk_fma_f32 v[28:29], v[44:45], v[28:29], v[28:29]
	v_rcp_f32_e64 v46, v46 clamp
	v_rcp_f32_e64 v47, v47 clamp
	v_rcp_f32_e64 v48, v48 clamp
	v_rcp_f32_e64 v49, v49 clamp
	v_rcp_f32_e64 v50, v50 clamp
	v_rcp_f32_e64 v51, v51 clamp
	v_rcp_f32_e64 v20, v20 clamp
	v_rcp_f32_e64 v21, v21 clamp
	v_rcp_f32_e64 v24, v24 clamp
	v_rcp_f32_e64 v25, v25 clamp
	v_rcp_f32_e64 v34, v34 clamp
	v_rcp_f32_e64 v35, v35 clamp
	v_rcp_f32_e64 v26, v26 clamp
	v_rcp_f32_e64 v27, v27 clamp
	v_rcp_f32_e64 v28, v28 clamp
	v_rcp_f32_e64 v29, v29 clamp
	v_pk_mul_f32 v[46:47], v[58:59], v[46:47]
	v_pk_mul_f32 v[48:49], v[60:61], v[48:49]
	v_pk_mul_f32 v[50:51], v[52:53], v[50:51]
	v_pk_mul_f32 v[20:21], v[22:23], v[20:21]
	v_pk_mul_f32 v[22:23], v[54:55], v[24:25]
	v_pk_mul_f32 v[24:25], v[56:57], v[34:35]
	v_pk_mul_f32 v[26:27], v[30:31], v[26:27]
	v_pk_mul_f32 v[28:29], v[32:33], v[28:29]
	v_pk_fma_f32 v[4:5], v[4:5], v[46:47], v[46:47]
	v_pk_fma_f32 v[6:7], v[6:7], v[48:49], v[48:49]
	v_pk_fma_f32 v[8:9], v[8:9], v[50:51], v[50:51]
	v_pk_fma_f32 v[10:11], v[10:11], v[20:21], v[20:21]
	v_pk_fma_f32 v[12:13], v[12:13], v[22:23], v[22:23]
	v_pk_fma_f32 v[18:19], v[18:19], v[24:25], v[24:25]
	v_pk_fma_f32 v[30:31], v[36:37], v[26:27], v[26:27]
	v_pk_fma_f32 v[32:33], v[44:45], v[28:29], v[28:29]
	s_nop 0
	v_pk_fma_f32 v[4:5], v[4:5], v[4:5], s[4:5] neg_lo:[1,0,0] neg_hi:[1,0,0] clamp
	v_pk_fma_f32 v[6:7], v[6:7], v[6:7], s[4:5] neg_lo:[1,0,0] neg_hi:[1,0,0] clamp
	v_pk_fma_f32 v[8:9], v[8:9], v[8:9], s[4:5] neg_lo:[1,0,0] neg_hi:[1,0,0] clamp
	v_pk_fma_f32 v[10:11], v[10:11], v[10:11], s[4:5] neg_lo:[1,0,0] neg_hi:[1,0,0] clamp
	v_pk_fma_f32 v[12:13], v[12:13], v[12:13], s[4:5] neg_lo:[1,0,0] neg_hi:[1,0,0] clamp
	v_pk_fma_f32 v[18:19], v[18:19], v[18:19], s[4:5] neg_lo:[1,0,0] neg_hi:[1,0,0] clamp
	v_pk_fma_f32 v[30:31], v[30:31], v[30:31], s[4:5] neg_lo:[1,0,0] neg_hi:[1,0,0] clamp
	s_nop 0
	v_pk_fma_f32 v[32:33], v[32:33], v[32:33], s[4:5] neg_lo:[1,0,0] neg_hi:[1,0,0] clamp
	s_nop 0
	v_pk_fma_f32 v[8:9], v[8:9], v[8:9], s[8:9] op_sel_hi:[1,1,0]
	v_pk_fma_f32 v[10:11], v[10:11], v[10:11], s[8:9] op_sel_hi:[1,1,0]
	v_pk_fma_f32 v[12:13], v[12:13], v[12:13], s[8:9] op_sel_hi:[1,1,0]
	v_pk_fma_f32 v[18:19], v[18:19], v[18:19], s[8:9] op_sel_hi:[1,1,0]
	v_pk_fma_f32 v[32:33], v[32:33], v[32:33], s[8:9] op_sel_hi:[1,1,0]
	v_pk_fma_f32 v[4:5], v[4:5], v[4:5], s[8:9] op_sel_hi:[1,1,0]
	v_pk_fma_f32 v[6:7], v[6:7], v[6:7], s[8:9] op_sel_hi:[1,1,0]
	v_pk_fma_f32 v[30:31], v[30:31], v[30:31], s[8:9] op_sel_hi:[1,1,0]
	v_pk_mul_f32 v[8:9], v[50:51], v[8:9]
	v_pk_mul_f32 v[84:85], v[20:21], v[10:11]
	v_pk_mul_f32 v[86:87], v[22:23], v[12:13]
	v_pk_mul_f32 v[10:11], v[24:25], v[18:19]
	v_pk_mul_f32 v[12:13], v[28:29], v[32:33]
	v_pk_mul_f32 v[64:65], v[46:47], v[4:5]
	v_pk_mul_f32 v[82:83], v[48:49], v[6:7]
	v_pk_mul_f32 v[20:21], v[30:31], v[26:27]
	ds_read_b128 v[4:7], v72 offset:6144
	ds_read_b128 v[22:25], v71 offset:42368
	ds_read_b128 v[26:29], v72 offset:7168
	ds_read_b128 v[30:33], v71 offset:42432
	v_cvt_pk_f16_f32 v19, v84, v85
	v_cvt_pk_f16_f32 v18, v8, v9
	v_cvt_pk_f16_f32 v20, v20, v21
	s_waitcnt lgkmcnt(2)
	v_mfma_f32_16x16x32_f16 v[34:37], v[4:7], v[14:17], v[22:25]
	v_cvt_pk_f16_f32 v21, v12, v13
	v_mfma_f32_16x16x32_f16 v[44:47], v[4:7], v[0:3], v[22:25]
	ds_read_b128 v[4:7], v72 offset:8192
	ds_read_b128 v[48:51], v71 offset:42496
	s_waitcnt lgkmcnt(2)
	v_cvt_pk_f16_f32 v22, v64, v65
	v_mfma_f32_16x16x32_f16 v[52:55], v[26:29], v[14:17], v[30:33]
	v_cvt_pk_f16_f32 v23, v82, v83
	v_cvt_pk_f16_f32 v24, v86, v87
	v_mfma_f32_16x16x32_f16 v[26:29], v[26:29], v[0:3], v[30:33]
	ds_read_b128 v[56:59], v71 offset:42560
	v_exp_f32_e32 v86, v34
	v_exp_f32_e32 v87, v35
	s_waitcnt lgkmcnt(1)
	v_mfma_f32_16x16x32_f16 v[60:63], v[4:7], v[14:17], v[48:51]
	ds_read_b128 v[30:33], v72 offset:9216
	v_exp_f32_e64 v88, v52 clamp
	v_exp_f32_e64 v89, v53 clamp
	v_exp_f32_e64 v90, v54 clamp
	v_mfma_f32_16x16x32_f16 v[48:51], v[4:7], v[0:3], v[48:51]
	ds_read_b128 v[64:67], v72 offset:10240
	ds_read_b128 v[74:77], v71 offset:42624
	s_nop 1
	v_exp_f32_e32 v4, v60
	s_waitcnt lgkmcnt(2)
	v_mfma_f32_16x16x32_f16 v[78:81], v[30:33], v[14:17], v[56:59]
	v_exp_f32_e32 v5, v61
	v_exp_f32_e32 v60, v36
	v_exp_f32_e32 v61, v37
	v_mfma_f32_16x16x32_f16 v[30:33], v[30:33], v[0:3], v[56:59]
	ds_read_b128 v[82:85], v71 offset:42688
	v_exp_f32_e64 v91, v55 clamp
	v_exp_f32_e32 v6, v62
	s_waitcnt lgkmcnt(1)
	v_mfma_f32_16x16x32_f16 v[34:37], v[64:67], v[14:17], v[74:77]
	ds_read_b128 v[56:59], v72 offset:11264
	v_exp_f32_e32 v7, v63
	v_exp_f32_e32 v8, v48
	v_exp_f32_e32 v9, v49
	v_mfma_f32_16x16x32_f16 v[52:55], v[64:67], v[0:3], v[74:77]
	v_exp_f32_e32 v44, v44
	v_exp_f32_e32 v45, v45
	v_exp_f32_e64 v26, v26 clamp
	s_waitcnt lgkmcnt(0)
	v_mfma_f32_16x16x32_f16 v[14:17], v[56:59], v[14:17], v[82:85]
	v_exp_f32_e64 v27, v27 clamp
	v_exp_f32_e32 v46, v46
	v_exp_f32_e32 v47, v47
	v_mfma_f32_16x16x32_f16 v[56:59], v[56:59], v[0:3], v[82:85]
	v_exp_f32_e64 v28, v28 clamp
	s_nop 2
	v_exp_f32_e32 v2, v14
	v_exp_f32_e32 v3, v15
	v_exp_f32_e32 v14, v16
	v_exp_f32_e32 v15, v17
	v_exp_f32_e32 v16, v30
	v_exp_f32_e32 v17, v31
	v_exp_f32_e64 v29, v29 clamp
	v_exp_f32_e32 v0, v50
	v_exp_f32_e32 v1, v51
	v_exp_f32_e32 v48, v78
	v_exp_f32_e32 v49, v79
	v_exp_f32_e64 v34, v34 clamp
	v_exp_f32_e64 v35, v35 clamp
	v_exp_f32_e32 v50, v80
	v_exp_f32_e32 v51, v81
	v_exp_f32_e64 v36, v36 clamp
	v_exp_f32_e64 v37, v37 clamp
	v_exp_f32_e64 v30, v52 clamp
	v_exp_f32_e64 v31, v53 clamp
	v_exp_f32_e32 v52, v56
	v_exp_f32_e32 v53, v57
	v_exp_f32_e32 v32, v32
	v_exp_f32_e32 v33, v33
	v_exp_f32_e64 v54, v54 clamp
	v_exp_f32_e64 v55, v55 clamp
	v_exp_f32_e32 v56, v58
	v_cvt_pk_f16_f32 v25, v10, v11
	v_exp_f32_e32 v57, v59
	v_pk_fma_f32 v[30:31], v[30:31], s[2:3], 1.0 op_sel_hi:[1,0,0]
	v_pk_fma_f32 v[10:11], v[88:89], s[2:3], 1.0 op_sel_hi:[1,0,0]
	v_pk_fma_f32 v[12:13], v[90:91], s[2:3], 1.0 op_sel_hi:[1,0,0]
	v_pk_fma_f32 v[26:27], v[26:27], s[2:3], 1.0 op_sel_hi:[1,0,0]
	v_pk_fma_f32 v[28:29], v[28:29], s[2:3], 1.0 op_sel_hi:[1,0,0]
	v_pk_fma_f32 v[34:35], v[34:35], s[2:3], 1.0 op_sel_hi:[1,0,0]
	v_pk_fma_f32 v[36:37], v[36:37], s[2:3], 1.0 op_sel_hi:[1,0,0]
	v_pk_fma_f32 v[54:55], v[54:55], s[2:3], 1.0 op_sel_hi:[1,0,0]
	v_pk_fma_f32 v[16:17], v[16:17], v[30:31], v[30:31]
	v_pk_fma_f32 v[58:59], v[86:87], v[10:11], v[10:11]
	v_pk_fma_f32 v[10:11], v[10:11], s[6:7], v[40:41] op_sel_hi:[1,0,0] neg_lo:[1,0,0] neg_hi:[1,0,0]
	v_pk_fma_f32 v[60:61], v[60:61], v[12:13], v[12:13]
	v_pk_fma_f32 v[12:13], v[12:13], s[6:7], v[40:41] op_sel_hi:[1,0,0] neg_lo:[1,0,0] neg_hi:[1,0,0]
	v_pk_fma_f32 v[44:45], v[44:45], v[26:27], v[26:27]
	v_pk_fma_f32 v[46:47], v[46:47], v[28:29], v[28:29]
	v_pk_fma_f32 v[48:49], v[48:49], v[34:35], v[34:35]
	v_pk_fma_f32 v[50:51], v[50:51], v[36:37], v[36:37]
	v_pk_fma_f32 v[32:33], v[32:33], v[54:55], v[54:55]
	v_pk_fma_f32 v[16:17], v[52:53], v[16:17], v[16:17]
	v_pk_fma_f32 v[26:27], v[26:27], s[6:7], v[40:41] op_sel_hi:[1,0,0] neg_lo:[1,0,0] neg_hi:[1,0,0]
	v_pk_fma_f32 v[28:29], v[28:29], s[6:7], v[40:41] op_sel_hi:[1,0,0] neg_lo:[1,0,0] neg_hi:[1,0,0]
	v_pk_fma_f32 v[34:35], v[34:35], s[6:7], v[40:41] op_sel_hi:[1,0,0] neg_lo:[1,0,0] neg_hi:[1,0,0]
	v_pk_fma_f32 v[36:37], v[36:37], s[6:7], v[40:41] op_sel_hi:[1,0,0] neg_lo:[1,0,0] neg_hi:[1,0,0]
	v_pk_fma_f32 v[30:31], v[30:31], s[6:7], v[40:41] op_sel_hi:[1,0,0] neg_lo:[1,0,0] neg_hi:[1,0,0]
	v_pk_fma_f32 v[54:55], v[54:55], s[6:7], v[40:41] op_sel_hi:[1,0,0] neg_lo:[1,0,0] neg_hi:[1,0,0]
	v_pk_fma_f32 v[58:59], v[4:5], v[58:59], v[58:59]
	v_pk_fma_f32 v[60:61], v[6:7], v[60:61], v[60:61]
	v_pk_fma_f32 v[44:45], v[8:9], v[44:45], v[44:45]
	v_pk_fma_f32 v[46:47], v[0:1], v[46:47], v[46:47]
	v_pk_fma_f32 v[48:49], v[2:3], v[48:49], v[48:49]
	v_pk_fma_f32 v[50:51], v[14:15], v[50:51], v[50:51]
	v_pk_fma_f32 v[32:33], v[56:57], v[32:33], v[32:33]
	v_rcp_f32_e64 v16, v16 clamp
	v_rcp_f32_e64 v17, v17 clamp
	v_rcp_f32_e64 v58, v58 clamp
	v_rcp_f32_e64 v59, v59 clamp
	v_rcp_f32_e64 v60, v60 clamp
	v_rcp_f32_e64 v61, v61 clamp
	v_rcp_f32_e64 v44, v44 clamp
	v_rcp_f32_e64 v45, v45 clamp
	v_rcp_f32_e64 v46, v46 clamp
	v_rcp_f32_e64 v47, v47 clamp
	v_rcp_f32_e64 v48, v48 clamp
	v_rcp_f32_e64 v49, v49 clamp
	v_rcp_f32_e64 v50, v50 clamp
	v_rcp_f32_e64 v51, v51 clamp
	v_rcp_f32_e64 v32, v32 clamp
	v_rcp_f32_e64 v33, v33 clamp
	v_pk_mul_f32 v[10:11], v[10:11], v[58:59]
	v_pk_mul_f32 v[12:13], v[12:13], v[60:61]
	v_pk_mul_f32 v[26:27], v[26:27], v[44:45]
	v_pk_mul_f32 v[34:35], v[34:35], v[48:49]
	v_pk_mul_f32 v[36:37], v[36:37], v[50:51]
	v_pk_mul_f32 v[28:29], v[28:29], v[46:47]
	v_pk_mul_f32 v[16:17], v[30:31], v[16:17]
	v_pk_mul_f32 v[30:31], v[54:55], v[32:33]
	v_pk_fma_f32 v[4:5], v[4:5], v[10:11], v[10:11]
	v_pk_fma_f32 v[6:7], v[6:7], v[12:13], v[12:13]
	v_pk_fma_f32 v[8:9], v[8:9], v[26:27], v[26:27]
	v_pk_fma_f32 v[2:3], v[2:3], v[34:35], v[34:35]
	v_pk_fma_f32 v[14:15], v[14:15], v[36:37], v[36:37]
	v_pk_fma_f32 v[0:1], v[0:1], v[28:29], v[28:29]
	v_pk_fma_f32 v[32:33], v[52:53], v[16:17], v[16:17]
	v_pk_fma_f32 v[44:45], v[56:57], v[30:31], v[30:31]
	s_nop 0
	v_pk_fma_f32 v[4:5], v[4:5], v[4:5], s[4:5] neg_lo:[1,0,0] neg_hi:[1,0,0] clamp
	v_pk_fma_f32 v[6:7], v[6:7], v[6:7], s[4:5] neg_lo:[1,0,0] neg_hi:[1,0,0] clamp
	v_pk_fma_f32 v[8:9], v[8:9], v[8:9], s[4:5] neg_lo:[1,0,0] neg_hi:[1,0,0] clamp
	v_pk_fma_f32 v[0:1], v[0:1], v[0:1], s[4:5] neg_lo:[1,0,0] neg_hi:[1,0,0] clamp
	v_pk_fma_f32 v[2:3], v[2:3], v[2:3], s[4:5] neg_lo:[1,0,0] neg_hi:[1,0,0] clamp
	v_pk_fma_f32 v[14:15], v[14:15], v[14:15], s[4:5] neg_lo:[1,0,0] neg_hi:[1,0,0] clamp
	v_pk_fma_f32 v[32:33], v[32:33], v[32:33], s[4:5] neg_lo:[1,0,0] neg_hi:[1,0,0] clamp
	s_nop 0
	v_pk_fma_f32 v[44:45], v[44:45], v[44:45], s[4:5] neg_lo:[1,0,0] neg_hi:[1,0,0] clamp
	s_nop 0
	v_pk_fma_f32 v[32:33], v[32:33], v[32:33], s[8:9] op_sel_hi:[1,1,0]
	v_pk_fma_f32 v[4:5], v[4:5], v[4:5], s[8:9] op_sel_hi:[1,1,0]
	v_pk_fma_f32 v[6:7], v[6:7], v[6:7], s[8:9] op_sel_hi:[1,1,0]
	v_pk_fma_f32 v[8:9], v[8:9], v[8:9], s[8:9] op_sel_hi:[1,1,0]
	v_pk_fma_f32 v[0:1], v[0:1], v[0:1], s[8:9] op_sel_hi:[1,1,0]
	v_pk_fma_f32 v[2:3], v[2:3], v[2:3], s[8:9] op_sel_hi:[1,1,0]
	v_pk_fma_f32 v[14:15], v[14:15], v[14:15], s[8:9] op_sel_hi:[1,1,0]
	v_pk_fma_f32 v[44:45], v[44:45], v[44:45], s[8:9] op_sel_hi:[1,1,0]
	v_pk_mul_f32 v[16:17], v[32:33], v[16:17]
	v_pk_mul_f32 v[52:53], v[10:11], v[4:5]
	v_pk_mul_f32 v[54:55], v[12:13], v[6:7]
	v_pk_mul_f32 v[26:27], v[26:27], v[8:9]
	v_pk_mul_f32 v[28:29], v[28:29], v[0:1]
	v_pk_mul_f32 v[56:57], v[34:35], v[2:3]
	v_pk_mul_f32 v[58:59], v[36:37], v[14:15]
	v_pk_mul_f32 v[60:61], v[30:31], v[44:45]
	s_cmp_lt_u32 s33, 8
	s_cbranch_scc0 .Lprio_half_out

.LBB0_35:
	s_cmp_lt_u32 s33, 5
	s_cbranch_scc0 .Lprio_late
	s_setprio 3

.Lprio_late:
	s_setprio 2
	s_cmp_lt_u32 s33, 6
	s_cbranch_scc1 .Lprio_done
	s_setprio 1
	s_cmp_lt_u32 s33, 8
	s_cbranch_scc1 .Lprio_done
	s_setprio 0
	s_branch .Lprio_done
.Lprio_half_out:
	s_setprio 0
	s_branch .Lprio_half
